# speedup vs baseline: 1.0113x; 1.0044x over previous
.LBB3_63:
	s_cmp_eq_u32 s14, s50
	s_cbranch_scc1 .Lgru_dump
	s_and_saveexec_b64 s[0:1], s[6:7]
	s_xor_b64 s[0:1], exec, s[0:1]
	s_cbranch_execz .LBB3_66
	s_and_b32 s21, s14, 1
	s_mulk_i32 s21, 0x1e00
	v_add_u32_e32 v231, s21, v211
	ds_read_b128 v[166:169], v231
	s_cmp_lt_u32 s14, 2
	s_cbranch_scc1 .LBB3_66
	v_exp_f32_e32 v0, v2
	v_exp_f32_e32 v2, v3
	v_exp_f32_e32 v3, v4
	v_exp_f32_e32 v4, v5
	v_exp_f32_e32 v5, v6
	v_exp_f32_e32 v6, v7
	v_exp_f32_e32 v7, v8
	v_exp_f32_e32 v8, v9
	v_exp_f32_e32 v9, v10
	v_exp_f32_e32 v10, v11
	v_exp_f32_e32 v11, v12
	v_exp_f32_e32 v12, v13
	v_exp_f32_e32 v13, v14
	v_add_f32_e32 v0, 1.0, v0
	v_exp_f32_e32 v14, v18
	v_exp_f32_e32 v18, v19
	v_exp_f32_e32 v19, v20
	v_exp_f32_e32 v20, v21
	v_exp_f32_e32 v21, v22
	v_exp_f32_e32 v22, v23
	v_exp_f32_e32 v23, v24
	v_exp_f32_e32 v24, v25
	v_exp_f32_e32 v25, v26
	v_exp_f32_e32 v26, v27
	v_exp_f32_e32 v27, v28
	v_exp_f32_e32 v28, v29
	v_exp_f32_e32 v29, v30
	v_add_f32_e32 v30, 1.0, v2
	v_add_f32_e32 v65, 1.0, v11
	v_rcp_f32_e32 v2, v0
	v_add_f32_e32 v79, 1.0, v12
	v_rcp_f32_e32 v12, v65
	v_add_f32_e32 v31, 1.0, v3
	v_rcp_f32_e32 v3, v30
	v_add_f32_e32 v47, 1.0, v6
	v_add_f32_e32 v80, 1.0, v13
	v_rcp_f32_e32 v13, v79
	v_add_f32_e32 v32, 1.0, v4
	v_add_f32_e32 v48, 1.0, v7
	v_rcp_f32_e32 v4, v31
	v_rcp_f32_e32 v7, v47
	v_fma_f32 v0, v2, v34, v66
	v_add_f32_e32 v81, 1.0, v14
	v_rcp_f32_e32 v14, v80
	v_fma_f32 v66, v12, v44, v76
	v_exp_f32_e32 v0, v0
	v_add_f32_e32 v33, 1.0, v5
	v_add_f32_e32 v49, 1.0, v8
	v_rcp_f32_e32 v5, v32
	v_rcp_f32_e32 v8, v48
	v_fma_f32 v31, v3, v35, v67
	v_exp_f32_e32 v66, v66
	v_fma_f32 v67, v13, v45, v77
	v_exp_f32_e32 v31, v31
	v_rcp_f32_e32 v6, v33
	v_fma_f32 v32, v4, v36, v68
	v_fma_f32 v48, v7, v39, v71
	v_exp_f32_e32 v67, v67
	v_fma_f32 v68, v14, v46, v78
	v_exp_f32_e32 v32, v32
	v_exp_f32_e32 v48, v48
	v_add_f32_e32 v0, 1.0, v0
	v_add_f32_e32 v63, 1.0, v9
	v_rcp_f32_e32 v9, v49
	v_fma_f32 v33, v5, v37, v69
	v_fma_f32 v49, v8, v40, v72
	v_exp_f32_e32 v68, v68
	v_add_f32_e32 v76, 1.0, v66
	v_rcp_f32_e32 v66, v0
	v_exp_f32_e32 v33, v33
	v_exp_f32_e32 v49, v49
	v_add_f32_e32 v31, 1.0, v31
	v_fma_f32 v47, v6, v38, v70
	v_add_f32_e32 v77, 1.0, v67
	v_rcp_f32_e32 v67, v31
	v_add_f32_e32 v219, 1.0, v18
	v_rcp_f32_e32 v18, v81
	v_exp_f32_e32 v47, v47
	v_add_f32_e32 v32, 1.0, v32
	v_add_f32_e32 v48, 1.0, v48
	v_add_f32_e32 v78, 1.0, v68
	v_rcp_f32_e32 v68, v32
	v_rcp_f32_e32 v71, v48
	v_fma_f32 v66, v66, -2.0, 1.0
	v_add_f32_e32 v220, 1.0, v19
	v_rcp_f32_e32 v19, v219
	v_add_f32_e32 v33, 1.0, v33
	v_add_f32_e32 v49, 1.0, v49
	v_add_f32_e32 v64, 1.0, v10
	v_sub_f32_e32 v0, v50, v66
	v_rcp_f32_e32 v10, v63
	v_rcp_f32_e32 v69, v33
	v_rcp_f32_e32 v72, v49
	v_fma_f32 v67, v67, -2.0, 1.0
	v_add_f32_e32 v221, 1.0, v20
	v_rcp_f32_e32 v20, v220
	v_add_f32_e32 v47, 1.0, v47
	v_fma_f32 v50, v18, v0, v66
	v_rcp_f32_e32 v11, v64
	v_sub_f32_e32 v0, v51, v67
	v_fma_f32 v63, v9, v41, v73
	v_rcp_f32_e32 v70, v47
	v_fma_f32 v68, v68, -2.0, 1.0
	v_add_f32_e32 v222, 1.0, v21
	v_rcp_f32_e32 v21, v221
	v_exp_f32_e32 v63, v63
	v_fma_f32 v51, v19, v0, v67
	v_fma_f32 v64, v10, v42, v74
	v_sub_f32_e32 v0, v52, v68
	v_fma_f32 v69, v69, -2.0, 1.0
	v_add_f32_e32 v223, 1.0, v22
	v_rcp_f32_e32 v22, v222
	v_exp_f32_e32 v64, v64
	v_fma_f32 v52, v20, v0, v68
	v_fma_f32 v65, v11, v43, v75
	v_sub_f32_e32 v0, v53, v69
	v_fma_f32 v70, v70, -2.0, 1.0
	v_add_f32_e32 v224, 1.0, v23
	v_rcp_f32_e32 v23, v223
	v_exp_f32_e32 v65, v65
	v_add_f32_e32 v63, 1.0, v63
	v_fma_f32 v53, v21, v0, v69
	v_rcp_f32_e32 v73, v63
	v_sub_f32_e32 v0, v54, v70
	v_fma_f32 v71, v71, -2.0, 1.0
	v_add_f32_e32 v225, 1.0, v24
	v_rcp_f32_e32 v24, v224
	v_add_f32_e32 v64, 1.0, v64
	v_fma_f32 v54, v22, v0, v70
	v_rcp_f32_e32 v74, v64
	v_sub_f32_e32 v0, v55, v71
	v_fma_f32 v72, v72, -2.0, 1.0
	v_add_f32_e32 v226, 1.0, v25
	v_rcp_f32_e32 v25, v225
	v_add_f32_e32 v65, 1.0, v65
	v_fma_f32 v55, v23, v0, v71
	v_rcp_f32_e32 v75, v65
	v_sub_f32_e32 v0, v56, v72
	v_fma_f32 v73, v73, -2.0, 1.0
	v_add_f32_e32 v227, 1.0, v26
	v_rcp_f32_e32 v26, v226
	v_fma_f32 v56, v24, v0, v72
	v_rcp_f32_e32 v76, v76
	v_sub_f32_e32 v0, v57, v73
	v_fma_f32 v74, v74, -2.0, 1.0
	v_add_f32_e32 v228, 1.0, v27
	v_rcp_f32_e32 v27, v227
	v_fma_f32 v57, v25, v0, v73
	v_rcp_f32_e32 v77, v77
	v_sub_f32_e32 v0, v58, v74
	v_fma_f32 v75, v75, -2.0, 1.0
	v_add_f32_e32 v229, 1.0, v28
	v_rcp_f32_e32 v28, v228
	v_fma_f32 v58, v26, v0, v74
	v_rcp_f32_e32 v78, v78
	v_sub_f32_e32 v0, v59, v75
	v_fma_f32 v76, v76, -2.0, 1.0
	v_add_f32_e32 v230, 1.0, v29
	v_rcp_f32_e32 v29, v229
	v_fma_f32 v59, v27, v0, v75
	v_rcp_f32_e32 v30, v230
	v_sub_f32_e32 v0, v60, v76
	v_fma_f32 v77, v77, -2.0, 1.0
	v_fma_f32 v60, v28, v0, v76
	v_fma_f32 v78, v78, -2.0, 1.0
	v_sub_f32_e32 v0, v61, v77
	s_nop 0
	v_fma_f32 v61, v29, v0, v77
	v_sub_f32_e32 v0, v62, v78
	s_nop 0
	v_fma_f32 v62, v30, v0, v78
	v_cvt_pk_f16_f32 v33, v52, v53
	v_cvt_f16_f32_e32 v0, v62
	v_cvt_pk_f16_f32 v32, v50, v51
	v_cvt_pk_f16_f32 v49, v56, v57
	v_cvt_pk_f16_f32 v48, v54, v55
	ds_write2_b64 v210, v[32:33], v[48:49] offset1:2
	v_cvt_pk_f16_f32 v33, v60, v61
	v_cvt_pk_f16_f32 v32, v58, v59
	v_perm_b32 v0, v208, v0, s15
	ds_write_b64 v210, v[32:33] offset:32
	ds_write_b64 v218, v[0:1]

.LBB3_78:
	s_andn2_b64 vcc, exec, s[8:9]
	s_cbranch_vccnz .LBB3_80
	s_setprio 1
	ds_read_b128 v[220:223], v215 offset:15360
	ds_read_b128 v[170:173], v231 offset:32
	ds_read_b128 v[174:177], v231 offset:64
	ds_read_b128 v[178:181], v231 offset:96
	ds_read_b128 v[182:185], v231 offset:128
	ds_read_b128 v[186:189], v231 offset:160
	ds_read_b128 v[196:199], v231 offset:192
	v_mfma_f32_32x32x16_f16 v[2:17], v[232:235], v[166:169], 0
	v_mfma_f32_32x32x16_f16 v[18:33], v[236:239], v[166:169], 0
	ds_read_b128 v[232:235], v215 offset:2048
	v_mfma_f32_32x32x16_f16 v[66:81], v[240:243], v[166:169], 0
	ds_read_b128 v[236:239], v215 offset:9216
	s_waitcnt lgkmcnt(7)
	v_mfma_f32_32x32x16_f16 v[2:17], v[244:247], v[170:173], v[2:17]
	ds_read_b128 v[240:243], v215 offset:16384
	v_mfma_f32_32x32x16_f16 v[18:33], v[200:203], v[170:173], v[18:33]
	ds_read_b128 v[244:247], v215 offset:3072
	ds_read_b128 v[166:169], v216
	v_mfma_f32_32x32x16_f16 v[66:81], v[220:223], v[170:173], v[66:81]
	ds_read_b128 v[200:203], v215 offset:10240
	s_waitcnt lgkmcnt(5)
	v_mfma_f32_32x32x16_f16 v[2:17], v[232:235], v[174:177], v[2:17]
	ds_read_b128 v[220:223], v215 offset:17408
	s_waitcnt lgkmcnt(5)
	v_mfma_f32_32x32x16_f16 v[18:33], v[236:239], v[174:177], v[18:33]
	ds_read_b128 v[232:235], v215 offset:4096
	ds_read_b128 v[170:173], v216 offset:32
	s_waitcnt lgkmcnt(6)
	v_mfma_f32_32x32x16_f16 v[66:81], v[240:243], v[174:177], v[66:81]
	ds_read_b128 v[236:239], v215 offset:11264
	s_waitcnt lgkmcnt(6)
	v_mfma_f32_32x32x16_f16 v[2:17], v[244:247], v[178:181], v[2:17]
	ds_read_b128 v[240:243], v215 offset:18432
	s_waitcnt lgkmcnt(5)
	v_mfma_f32_32x32x16_f16 v[18:33], v[200:203], v[178:181], v[18:33]
	ds_read_b128 v[244:247], v215 offset:5120
	ds_read_b128 v[174:177], v216 offset:64
	s_waitcnt lgkmcnt(6)
	v_mfma_f32_32x32x16_f16 v[66:81], v[220:223], v[178:181], v[66:81]
	ds_read_b128 v[200:203], v215 offset:12288
	s_waitcnt lgkmcnt(6)
	v_mfma_f32_32x32x16_f16 v[2:17], v[232:235], v[182:185], v[2:17]
	ds_read_b128 v[220:223], v215 offset:19456
	s_waitcnt lgkmcnt(5)
	v_mfma_f32_32x32x16_f16 v[18:33], v[236:239], v[182:185], v[18:33]
	ds_read_b128 v[232:235], v215 offset:6144
	ds_read_b128 v[178:181], v216 offset:96
	s_waitcnt lgkmcnt(6)
	v_mfma_f32_32x32x16_f16 v[66:81], v[240:243], v[182:185], v[66:81]
	ds_read_b128 v[236:239], v215 offset:13312
	s_waitcnt lgkmcnt(6)
	v_mfma_f32_32x32x16_f16 v[2:17], v[244:247], v[186:189], v[2:17]
	ds_read_b128 v[240:243], v215 offset:20480
	s_waitcnt lgkmcnt(5)
	v_mfma_f32_32x32x16_f16 v[18:33], v[200:203], v[186:189], v[18:33]
	ds_read_b128 v[182:185], v216 offset:128
	s_waitcnt lgkmcnt(5)
	v_mfma_f32_32x32x16_f16 v[66:81], v[220:223], v[186:189], v[66:81]
	s_waitcnt lgkmcnt(4)
	v_mfma_f32_32x32x16_f16 v[2:17], v[232:235], v[196:199], v[2:17]
	s_waitcnt lgkmcnt(2)
	v_mfma_f32_32x32x16_f16 v[18:33], v[236:239], v[196:199], v[18:33]
	ds_read_b128 v[186:189], v216 offset:160
	s_waitcnt lgkmcnt(2)
	v_mfma_f32_32x32x16_f16 v[66:81], v[240:243], v[196:199], v[66:81]
	v_mfma_f32_32x32x16_f16 v[2:17], v[82:85], v[166:169], v[2:17]
	v_mfma_f32_32x32x16_f16 v[18:33], v[130:133], v[166:169], v[18:33]
	ds_read_b128 v[196:199], v216 offset:192
	v_mfma_f32_32x32x16_f16 v[34:49], v[138:141], v[166:169], 0
	v_mfma_f32_32x32x16_f16 v[2:17], v[86:89], v[170:173], v[2:17]
	ds_read_b128 v[232:235], v215
	v_mfma_f32_32x32x16_f16 v[18:33], v[110:113], v[170:173], v[18:33]
	ds_read_b128 v[236:239], v215 offset:7168
	v_mfma_f32_32x32x16_f16 v[34:49], v[142:145], v[170:173], v[34:49]
	ds_read_b128 v[240:243], v215 offset:14336
	v_mfma_f32_32x32x16_f16 v[2:17], v[90:93], v[174:177], v[2:17]
	ds_read_b128 v[244:247], v215 offset:1024
	v_mfma_f32_32x32x16_f16 v[18:33], v[114:117], v[174:177], v[18:33]
	ds_read_b128 v[200:203], v215 offset:8192
	v_mfma_f32_32x32x16_f16 v[34:49], v[146:149], v[174:177], v[34:49]
	v_mfma_f32_32x32x16_f16 v[2:17], v[94:97], v[178:181], v[2:17]
	v_mfma_f32_32x32x16_f16 v[18:33], v[118:121], v[178:181], v[18:33]
	v_mfma_f32_32x32x16_f16 v[34:49], v[150:153], v[178:181], v[34:49]
	s_waitcnt lgkmcnt(7)
	v_mfma_f32_32x32x16_f16 v[2:17], v[106:109], v[182:185], v[2:17]
	v_mfma_f32_32x32x16_f16 v[18:33], v[122:125], v[182:185], v[18:33]
	v_mfma_f32_32x32x16_f16 v[34:49], v[154:157], v[182:185], v[34:49]
	s_waitcnt lgkmcnt(6)
	v_mfma_f32_32x32x16_f16 v[2:17], v[98:101], v[186:189], v[2:17]
	v_mfma_f32_32x32x16_f16 v[18:33], v[126:129], v[186:189], v[18:33]
	v_mfma_f32_32x32x16_f16 v[34:49], v[158:161], v[186:189], v[34:49]
	s_waitcnt lgkmcnt(5)
	v_mfma_f32_32x32x16_f16 v[2:17], v[102:105], v[196:199], v[2:17]
	v_mfma_f32_32x32x16_f16 v[18:33], v[134:137], v[196:199], v[18:33]
	v_mfma_f32_32x32x16_f16 v[34:49], v[162:165], v[196:199], v[34:49]
	s_setprio 0
